# v23 with the MLA late DMA issue point after the 2nd (instead of 4th) QK MFMA
# baseline (speedup 1.0000x reference)
; __device__ __forceinline__ void finishSM(f32x16& p0, f32x16& p1, float& l_reg, bf16x8& pa0, bf16x8& pa1, bf16x8& pa2, bf16x8& pa3) {
; #pragma unroll
;   for (int r = 0; r < 16; ++r) p1[r] = __builtin_amdgcn_exp2f(p1[r]);
;   float ps = 0;
; #pragma unroll
;   for (int r = 0; r < 16; ++r) ps += p0[r];
; #pragma unroll
;   for (int r = 0; r < 16; ++r) ps += p1[r];
;   l_reg += ps;
;     ...
;   ATT_PK4(p0, 0, pa0); ATT_PK4(p0, 8, pa1); ATT_PK4(p1, 0, pa2); ATT_PK4(p1, 8, pa3);
;     ...
; }
; template <int DK>
; __device__ __forceinline__ void qkt(f32x16& p0, f32x16& p1, const char* Ks, const bf16x8* qr, int r32, int hi) {
;   p0 = f32x16{}; p1 = f32x16{};
; #pragma unroll
;   for (int d0 = 0; d0 < DK / 16; ++d0) { const int cb = (d0 * 16 + hi * 8) * 2;
;     const bf16x8 b0 = *reinterpret_cast<const bf16x8*>(Ks + ATT_KSWZ(r32, cb));
;     const bf16x8 b1 = *reinterpret_cast<const bf16x8*>(Ks + ATT_KSWZ(32 + r32, cb));
;     p0 = __builtin_amdgcn_mfma_f32_32x32x16_bf16(b0, qr[d0], p0, 0, 0, 0);
;     p1 = __builtin_amdgcn_mfma_f32_32x32x16_bf16(b1, qr[d0], p1, 0, 0, 0);
;   }
.LBB0_1432:
	ds_read_b128 v[50:53], v126 offset:32768
	ds_read_b128 v[54:57], v126 offset:40960
	ds_read_b128 v[82:85], v127 offset:32768
	ds_read_b128 v[86:89], v127 offset:40960
	v_exp_f32_e32 v34, v34
	v_exp_f32_e32 v35, v35
	s_waitcnt lgkmcnt(0)
	v_mfma_f32_32x32x16_bf16 v[66:81], v[50:53], v[98:101], 0
	v_exp_f32_e32 v36, v36
	v_exp_f32_e32 v37, v37
	v_exp_f32_e32 v38, v38
	v_exp_f32_e32 v39, v39
	v_exp_f32_e32 v40, v40
	v_exp_f32_e32 v41, v41
	v_exp_f32_e32 v42, v42
	v_mfma_f32_32x32x16_bf16 v[50:65], v[54:57], v[98:101], 0
	s_cmp_eq_u32 s93, 0
	s_cbranch_scc1 .Lmstag_4
	s_add_i32 s32, s92, 5
	s_cmp_ge_u32 s32, s89
	s_cbranch_scc1 .Lmstag_4
	v_lshl_add_u64 v[240:241], v[92:93], 0, s[12:13]
	s_mov_b64 s[96:97], 0x2a81e000
	v_lshl_add_u64 v[240:241], v[240:241], 0, s[96:97]
	s_add_i32 m0, s81, 0x8000
	s_nop 0
	global_load_lds_dwordx4 v[240:241], off
	v_lshl_add_u64 v[240:241], v[94:95], 0, s[12:13]
	v_lshl_add_u64 v[240:241], v[240:241], 0, s[96:97]
	s_add_i32 m0, s81, 0x8400
	s_mov_b64 s[96:97], 0x30e14000
	global_load_lds_dwordx4 v[240:241], off
	v_lshl_add_u64 v[240:241], v[90:91], 0, s[12:13]
	v_lshl_add_u64 v[240:241], v[240:241], 0, s[96:97]
	s_add_i32 m0, s87, 0x4000
	s_nop 0
	global_load_lds_dwordx4 v[240:241], off
.Lmstag_4:
	v_exp_f32_e32 v43, v43
	v_exp_f32_e32 v44, v44
	v_exp_f32_e32 v45, v45
	v_exp_f32_e32 v46, v46
	v_exp_f32_e32 v47, v47
	v_exp_f32_e32 v48, v48
	v_exp_f32_e32 v49, v49
	v_mfma_f32_32x32x16_bf16 v[66:81], v[82:85], v[102:105], v[66:81]
	v_add_f32_e32 v0, 0, v184
	v_add_f32_e32 v0, v186, v0
	v_add_f32_e32 v0, v185, v0
	v_add_f32_e32 v0, v187, v0
	v_add_f32_e32 v0, v189, v0
	v_add_f32_e32 v0, v193, v0
	v_add_f32_e32 v0, v192, v0
	v_mfma_f32_32x32x16_bf16 v[50:65], v[86:89], v[102:105], v[50:65]
	ds_read_b128 v[82:85], v128 offset:32768
	ds_read_b128 v[86:89], v128 offset:40960
	v_add_f32_e32 v0, v194, v0
	v_add_f32_e32 v0, v188, v0
	v_add_f32_e32 v0, v191, v0
	v_add_f32_e32 v0, v190, v0
	v_add_f32_e32 v0, v196, v0
	v_add_f32_e32 v0, v195, v0
	s_waitcnt lgkmcnt(0)
	v_mfma_f32_32x32x16_bf16 v[66:81], v[82:85], v[106:109], v[66:81]
	v_add_f32_e32 v0, v198, v0
	v_add_f32_e32 v0, v197, v0
	v_add_f32_e32 v0, v199, v0
	v_add_f32_e32 v0, v34, v0
	v_add_f32_e32 v0, v35, v0
	v_add_f32_e32 v0, v36, v0
	v_add_f32_e32 v0, v37, v0
	v_mfma_f32_32x32x16_bf16 v[50:65], v[86:89], v[106:109], v[50:65]
	ds_read_b128 v[82:85], v129 offset:32768
	ds_read_b128 v[86:89], v129 offset:40960
	v_add_f32_e32 v0, v38, v0
	v_add_f32_e32 v0, v39, v0
	v_add_f32_e32 v0, v40, v0
	v_add_f32_e32 v0, v41, v0
	v_add_f32_e32 v0, v42, v0
	v_add_f32_e32 v0, v43, v0
	s_waitcnt lgkmcnt(0)
	v_mfma_f32_32x32x16_bf16 v[66:81], v[82:85], v[110:113], v[66:81]
	v_add_f32_e32 v0, v44, v0
	v_add_f32_e32 v0, v45, v0
	v_add_f32_e32 v0, v46, v0
	v_add_f32_e32 v0, v47, v0
	v_add_f32_e32 v0, v48, v0
	v_add_f32_e32 v0, v49, v0
	v_add_f32_e32 v145, v145, v0
	v_mfma_f32_32x32x16_bf16 v[50:65], v[86:89], v[110:113], v[50:65]
	ds_read_b128 v[82:85], v130 offset:32768
	ds_read_b128 v[86:89], v130 offset:40960
	s_waitcnt lgkmcnt(0)
	v_mfma_f32_32x32x16_bf16 v[66:81], v[82:85], v[114:117], v[66:81]
	v_mfma_f32_32x32x16_bf16 v[50:65], v[86:89], v[114:117], v[50:65]
	ds_read_b128 v[82:85], v131 offset:32768
	ds_read_b128 v[86:89], v131 offset:40960
	s_waitcnt lgkmcnt(0)
	v_mfma_f32_32x32x16_bf16 v[66:81], v[82:85], v[118:121], v[66:81]
	v_cvt_pk_bf16_f32 v82, v184, v186
	v_cvt_pk_bf16_f32 v83, v185, v187
	v_cvt_pk_bf16_f32 v84, v189, v193
	v_cvt_pk_bf16_f32 v85, v192, v194
	s_nop 0
	v_permlane32_swap_b32_e32 v82, v84
	v_mfma_f32_32x32x16_bf16 v[50:65], v[86:89], v[118:121], v[50:65]
	v_cvt_pk_bf16_f32 v86, v188, v191
	v_cvt_pk_bf16_f32 v87, v190, v196
	v_cvt_pk_bf16_f32 v88, v195, v198
	v_cvt_pk_bf16_f32 v89, v197, v199
	v_cvt_pk_bf16_f32 v122, v34, v35
	v_cvt_pk_bf16_f32 v123, v36, v37
	v_cvt_pk_bf16_f32 v124, v38, v39
	v_cvt_pk_bf16_f32 v125, v40, v41
	v_cvt_pk_bf16_f32 v150, v42, v43
	v_cvt_pk_bf16_f32 v151, v44, v45
	v_cvt_pk_bf16_f32 v152, v46, v47
	v_cvt_pk_bf16_f32 v153, v48, v49
	ds_read_b64_tr_b16 v[154:155], v96 offset:0
	ds_read_b64_tr_b16 v[156:157], v96 offset:0x400
	ds_read_b64_tr_b16 v[158:159], v96 offset:0x800
	ds_read_b64_tr_b16 v[160:161], v96 offset:0xc00
	ds_read_b64_tr_b16 v[162:163], v96 offset:0x1000
	ds_read_b64_tr_b16 v[164:165], v96 offset:0x1400
	ds_read_b64_tr_b16 v[166:167], v96 offset:0x1800
	ds_read_b64_tr_b16 v[168:169], v96 offset:0x1c00
	ds_read_b64_tr_b16 v[170:171], v96 offset:0x200
	ds_read_b64_tr_b16 v[172:173], v96 offset:0x600
	ds_read_b64_tr_b16 v[200:201], v96 offset:0xa00
	ds_read_b64_tr_b16 v[202:203], v96 offset:0xe00
	v_permlane32_swap_b32_e32 v83, v85
	ds_read_b64_tr_b16 v[204:205], v96 offset:0x1200
	ds_read_b64_tr_b16 v[206:207], v96 offset:0x1600
	ds_read_b64_tr_b16 v[208:209], v96 offset:0x1a00
	ds_read_b64_tr_b16 v[210:211], v96 offset:0x1e00
	s_waitcnt lgkmcnt(8)
	v_permlane32_swap_b32_e32 v86, v88
	s_nop 0
	v_mfma_f32_32x32x16_bf16 v[2:17], v[82:85], v[154:157], v[2:17]
	s_waitcnt lgkmcnt(0)
	v_permlane32_swap_b32_e32 v87, v89
	v_permlane32_swap_b32_e32 v122, v124
	v_permlane32_swap_b32_e32 v123, v125
	v_mfma_f32_32x32x16_bf16 v[18:33], v[82:85], v[170:173], v[18:33]
	v_permlane32_swap_b32_e32 v150, v152
	v_permlane32_swap_b32_e32 v151, v153
	v_exp_f32_e32 v170, v76
	v_exp_f32_e32 v171, v77
	v_exp_f32_e32 v172, v78
	v_mfma_f32_32x32x16_bf16 v[2:17], v[86:89], v[158:161], v[2:17]
	v_exp_f32_e32 v158, v66
	v_exp_f32_e32 v159, v67
	v_exp_f32_e32 v160, v68
	v_exp_f32_e32 v161, v69
	v_exp_f32_e32 v173, v79
	v_exp_f32_e32 v174, v80
	v_exp_f32_e32 v175, v81
	v_mfma_f32_32x32x16_bf16 v[18:33], v[86:89], v[200:203], v[18:33]
	v_mfma_f32_32x32x16_bf16 v[2:17], v[122:125], v[162:165], v[2:17]
	v_exp_f32_e32 v162, v70
	v_exp_f32_e32 v163, v71
	v_mfma_f32_32x32x16_bf16 v[18:33], v[122:125], v[204:207], v[18:33]
	v_mfma_f32_32x32x16_bf16 v[2:17], v[150:153], v[166:169], v[2:17]
	v_exp_f32_e32 v166, v72
	v_exp_f32_e32 v167, v73
	v_exp_f32_e32 v168, v74
	v_exp_f32_e32 v169, v75
	v_mfma_f32_32x32x16_bf16 v[18:33], v[150:153], v[208:211], v[18:33]

; __device__ __forceinline__ void finishSM(f32x16& p0, f32x16& p1, float& l_reg, bf16x8& pa0, bf16x8& pa1, bf16x8& pa2, bf16x8& pa3) {
; #pragma unroll
;   for (int r = 0; r < 16; ++r) p1[r] = __builtin_amdgcn_exp2f(p1[r]);
;   float ps = 0;
; #pragma unroll
;   for (int r = 0; r < 16; ++r) ps += p0[r];
; #pragma unroll
;   for (int r = 0; r < 16; ++r) ps += p1[r];
;   l_reg += ps;
;     ...
;   ATT_PK4(p0, 0, pa0); ATT_PK4(p0, 8, pa1); ATT_PK4(p1, 0, pa2); ATT_PK4(p1, 8, pa3);
;     ...
; }
; template <int DK>
; __device__ __forceinline__ void qkt(f32x16& p0, f32x16& p1, const char* Ks, const bf16x8* qr, int r32, int hi) {
;   p0 = f32x16{}; p1 = f32x16{};
; #pragma unroll
;   for (int d0 = 0; d0 < DK / 16; ++d0) { const int cb = (d0 * 16 + hi * 8) * 2;
;     const bf16x8 b0 = *reinterpret_cast<const bf16x8*>(Ks + ATT_KSWZ(r32, cb));
;     const bf16x8 b1 = *reinterpret_cast<const bf16x8*>(Ks + ATT_KSWZ(32 + r32, cb));
;     p0 = __builtin_amdgcn_mfma_f32_32x32x16_bf16(b0, qr[d0], p0, 0, 0, 0);
;     p1 = __builtin_amdgcn_mfma_f32_32x32x16_bf16(b1, qr[d0], p1, 0, 0, 0);
;   }
.LBB0_1440:
	ds_read_b128 v[34:37], v126 offset:49152
	ds_read_b128 v[38:41], v126 offset:57344
	ds_read_b128 v[82:85], v127 offset:49152
	ds_read_b128 v[86:89], v127 offset:57344
	v_exp_f32_e32 v50, v50
	v_exp_f32_e32 v51, v51
	s_waitcnt lgkmcnt(0)
	v_mfma_f32_32x32x16_bf16 v[66:81], v[34:37], v[98:101], 0
	v_exp_f32_e32 v52, v52
	v_exp_f32_e32 v53, v53
	v_exp_f32_e32 v54, v54
	v_exp_f32_e32 v55, v55
	v_exp_f32_e32 v56, v56
	v_exp_f32_e32 v57, v57
	v_exp_f32_e32 v58, v58
	v_mfma_f32_32x32x16_bf16 v[34:49], v[38:41], v[98:101], 0
	s_cmp_eq_u32 s93, 0
	s_cbranch_scc1 .Lmstag_1
	s_add_i32 s32, s92, 2
	s_cmp_ge_u32 s32, s89
	s_cbranch_scc1 .Lmstag_1
	v_lshl_add_u64 v[240:241], v[92:93], 0, s[12:13]
	s_mov_b64 s[96:97], 0x2a815000
	s_mov_b32 m0, s85
	v_lshl_add_u64 v[240:241], v[240:241], 0, s[96:97]
	global_load_lds_dwordx4 v[240:241], off
	v_lshl_add_u64 v[240:241], v[94:95], 0, s[12:13]
	v_lshl_add_u64 v[240:241], v[240:241], 0, s[96:97]
	s_mov_b32 m0, s86
	s_mov_b64 s[96:97], 0x30e0e000
	global_load_lds_dwordx4 v[240:241], off
	v_lshl_add_u64 v[240:241], v[90:91], 0, s[12:13]
	v_lshl_add_u64 v[240:241], v[240:241], 0, s[96:97]
	s_mov_b32 m0, s88
	s_nop 0
	global_load_lds_dwordx4 v[240:241], off
.Lmstag_1:
	v_exp_f32_e32 v59, v59
	v_exp_f32_e32 v60, v60
	v_exp_f32_e32 v61, v61
	v_exp_f32_e32 v62, v62
	v_exp_f32_e32 v63, v63
	v_exp_f32_e32 v64, v64
	v_exp_f32_e32 v65, v65
	v_mfma_f32_32x32x16_bf16 v[66:81], v[82:85], v[102:105], v[66:81]
	v_add_f32_e32 v0, 0, v158
	v_add_f32_e32 v0, v159, v0
	v_add_f32_e32 v0, v160, v0
	v_add_f32_e32 v0, v161, v0
	v_add_f32_e32 v0, v162, v0
	v_add_f32_e32 v0, v163, v0
	v_add_f32_e32 v0, v166, v0
	v_mfma_f32_32x32x16_bf16 v[34:49], v[86:89], v[102:105], v[34:49]
	ds_read_b128 v[82:85], v128 offset:49152
	ds_read_b128 v[86:89], v128 offset:57344
	v_add_f32_e32 v0, v167, v0
	v_add_f32_e32 v0, v168, v0
	v_add_f32_e32 v0, v169, v0
	v_add_f32_e32 v0, v170, v0
	v_add_f32_e32 v0, v171, v0
	v_add_f32_e32 v0, v172, v0
	s_waitcnt lgkmcnt(0)
	v_mfma_f32_32x32x16_bf16 v[66:81], v[82:85], v[106:109], v[66:81]
	v_add_f32_e32 v0, v173, v0
	v_add_f32_e32 v0, v174, v0
	v_add_f32_e32 v0, v175, v0
	v_add_f32_e32 v0, v50, v0
	v_add_f32_e32 v0, v51, v0
	v_add_f32_e32 v0, v52, v0
	v_add_f32_e32 v0, v53, v0
	v_mfma_f32_32x32x16_bf16 v[34:49], v[86:89], v[106:109], v[34:49]
	ds_read_b128 v[82:85], v129 offset:49152
	ds_read_b128 v[86:89], v129 offset:57344
	v_add_f32_e32 v0, v54, v0
	v_add_f32_e32 v0, v55, v0
	v_add_f32_e32 v0, v56, v0
	v_add_f32_e32 v0, v57, v0
	v_add_f32_e32 v0, v58, v0
	v_add_f32_e32 v0, v59, v0
	s_waitcnt lgkmcnt(0)
	v_mfma_f32_32x32x16_bf16 v[66:81], v[82:85], v[110:113], v[66:81]
	v_add_f32_e32 v0, v60, v0
	v_add_f32_e32 v0, v61, v0
	v_add_f32_e32 v0, v62, v0
	v_add_f32_e32 v0, v63, v0
	v_add_f32_e32 v0, v64, v0
	v_add_f32_e32 v0, v65, v0
	v_add_f32_e32 v145, v145, v0
	v_mfma_f32_32x32x16_bf16 v[34:49], v[86:89], v[110:113], v[34:49]
	ds_read_b128 v[82:85], v130 offset:49152
	ds_read_b128 v[86:89], v130 offset:57344
	s_andn2_b64 vcc, exec, s[38:39]
	s_waitcnt lgkmcnt(0)
	v_mfma_f32_32x32x16_bf16 v[66:81], v[82:85], v[114:117], v[66:81]
	v_mfma_f32_32x32x16_bf16 v[34:49], v[86:89], v[114:117], v[34:49]
	ds_read_b128 v[82:85], v131 offset:49152
	ds_read_b128 v[86:89], v131 offset:57344
	s_waitcnt lgkmcnt(0)
	v_mfma_f32_32x32x16_bf16 v[66:81], v[82:85], v[118:121], v[66:81]
	v_cvt_pk_bf16_f32 v82, v158, v159
	v_cvt_pk_bf16_f32 v83, v160, v161
	v_cvt_pk_bf16_f32 v84, v162, v163
	v_cvt_pk_bf16_f32 v85, v166, v167
	s_nop 0
	v_permlane32_swap_b32_e32 v82, v84
	v_mfma_f32_32x32x16_bf16 v[34:49], v[86:89], v[118:121], v[34:49]
	v_cvt_pk_bf16_f32 v86, v168, v169
	v_cvt_pk_bf16_f32 v87, v170, v171
	v_cvt_pk_bf16_f32 v88, v172, v173
	v_cvt_pk_bf16_f32 v89, v174, v175
	v_cvt_pk_bf16_f32 v122, v50, v51
	v_cvt_pk_bf16_f32 v123, v52, v53
	v_cvt_pk_bf16_f32 v124, v54, v55
	v_cvt_pk_bf16_f32 v125, v56, v57
	v_cvt_pk_bf16_f32 v150, v58, v59
	v_cvt_pk_bf16_f32 v151, v60, v61
	v_cvt_pk_bf16_f32 v152, v62, v63
	v_cvt_pk_bf16_f32 v153, v64, v65
	ds_read_b64_tr_b16 v[154:155], v132 offset:0
	ds_read_b64_tr_b16 v[156:157], v132 offset:0x400
	ds_read_b64_tr_b16 v[184:185], v132 offset:0x800
	ds_read_b64_tr_b16 v[186:187], v132 offset:0xc00
	ds_read_b64_tr_b16 v[188:189], v132 offset:0x1000
	ds_read_b64_tr_b16 v[190:191], v132 offset:0x1400
	ds_read_b64_tr_b16 v[192:193], v132 offset:0x1800
	ds_read_b64_tr_b16 v[194:195], v132 offset:0x1c00
	ds_read_b64_tr_b16 v[196:197], v132 offset:0x200
	ds_read_b64_tr_b16 v[198:199], v132 offset:0x600
	ds_read_b64_tr_b16 v[200:201], v132 offset:0xa00
	ds_read_b64_tr_b16 v[202:203], v132 offset:0xe00
	v_permlane32_swap_b32_e32 v83, v85
	ds_read_b64_tr_b16 v[204:205], v132 offset:0x1200
	ds_read_b64_tr_b16 v[206:207], v132 offset:0x1600
	ds_read_b64_tr_b16 v[208:209], v132 offset:0x1a00
	ds_read_b64_tr_b16 v[210:211], v132 offset:0x1e00
	s_waitcnt lgkmcnt(8)
	v_permlane32_swap_b32_e32 v86, v88
	s_nop 0
	v_mfma_f32_32x32x16_bf16 v[2:17], v[82:85], v[154:157], v[2:17]
	s_waitcnt lgkmcnt(0)
	v_permlane32_swap_b32_e32 v87, v89
	v_permlane32_swap_b32_e32 v122, v124
	v_permlane32_swap_b32_e32 v123, v125
	v_mfma_f32_32x32x16_bf16 v[18:33], v[82:85], v[196:199], v[18:33]
	v_permlane32_swap_b32_e32 v150, v152
	v_permlane32_swap_b32_e32 v151, v153
	v_exp_f32_e32 v196, v77
	v_exp_f32_e32 v198, v79
	v_exp_f32_e32 v197, v80
	v_mfma_f32_32x32x16_bf16 v[2:17], v[86:89], v[184:187], v[2:17]
	v_exp_f32_e32 v184, v66
	v_exp_f32_e32 v186, v67
	v_exp_f32_e32 v185, v68
	v_exp_f32_e32 v187, v69
	v_exp_f32_e32 v199, v81
	v_mfma_f32_32x32x16_bf16 v[18:33], v[86:89], v[200:203], v[18:33]
	v_mfma_f32_32x32x16_bf16 v[2:17], v[122:125], v[188:191], v[2:17]
	v_exp_f32_e32 v189, v70
	v_exp_f32_e32 v188, v74
	v_exp_f32_e32 v191, v75
	v_exp_f32_e32 v190, v76
	v_mfma_f32_32x32x16_bf16 v[18:33], v[122:125], v[204:207], v[18:33]
	v_mfma_f32_32x32x16_bf16 v[2:17], v[150:153], v[192:195], v[2:17]
	v_exp_f32_e32 v193, v71
	v_exp_f32_e32 v192, v72
	v_exp_f32_e32 v194, v73
	v_exp_f32_e32 v195, v78
	v_mfma_f32_32x32x16_bf16 v[18:33], v[150:153], v[208:211], v[18:33]
	s_cbranch_vccnz .LBB0_1449

; __device__ __forceinline__ void finishSM(f32x16& p0, f32x16& p1, float& l_reg, bf16x8& pa0, bf16x8& pa1, bf16x8& pa2, bf16x8& pa3) {
; #pragma unroll
;   for (int r = 0; r < 16; ++r) p1[r] = __builtin_amdgcn_exp2f(p1[r]);
;   float ps = 0;
; #pragma unroll
;   for (int r = 0; r < 16; ++r) ps += p0[r];
; #pragma unroll
;   for (int r = 0; r < 16; ++r) ps += p1[r];
;   l_reg += ps;
;     ...
;   ATT_PK4(p0, 0, pa0); ATT_PK4(p0, 8, pa1); ATT_PK4(p1, 0, pa2); ATT_PK4(p1, 8, pa3);
;     ...
; }
; template <int DK>
; __device__ __forceinline__ void qkt(f32x16& p0, f32x16& p1, const char* Ks, const bf16x8* qr, int r32, int hi) {
;   p0 = f32x16{}; p1 = f32x16{};
; #pragma unroll
;   for (int d0 = 0; d0 < DK / 16; ++d0) { const int cb = (d0 * 16 + hi * 8) * 2;
;     const bf16x8 b0 = *reinterpret_cast<const bf16x8*>(Ks + ATT_KSWZ(r32, cb));
;     const bf16x8 b1 = *reinterpret_cast<const bf16x8*>(Ks + ATT_KSWZ(32 + r32, cb));
;     p0 = __builtin_amdgcn_mfma_f32_32x32x16_bf16(b0, qr[d0], p0, 0, 0, 0);
;     p1 = __builtin_amdgcn_mfma_f32_32x32x16_bf16(b1, qr[d0], p1, 0, 0, 0);
;   }
.LBB0_1447:
	ds_read_b128 v[50:53], v133
	ds_read_b128 v[54:57], v133 offset:8192
	ds_read_b128 v[82:85], v134
	ds_read_b128 v[86:89], v134 offset:8192
	v_exp_f32_e32 v34, v34
	v_exp_f32_e32 v35, v35
	s_waitcnt lgkmcnt(0)
	v_mfma_f32_32x32x16_bf16 v[66:81], v[50:53], v[98:101], 0
	v_exp_f32_e32 v36, v36
	v_exp_f32_e32 v37, v37
	v_exp_f32_e32 v38, v38
	v_exp_f32_e32 v39, v39
	v_exp_f32_e32 v40, v40
	v_exp_f32_e32 v41, v41
	v_exp_f32_e32 v42, v42
	v_mfma_f32_32x32x16_bf16 v[50:65], v[54:57], v[98:101], 0
	s_cmp_eq_u32 s93, 0
	s_cbranch_scc1 .Lmstag_2
	s_add_i32 s32, s92, 3
	s_cmp_ge_u32 s32, s89
	s_cbranch_scc1 .Lmstag_2
	v_lshl_add_u64 v[240:241], v[92:93], 0, s[12:13]
	s_mov_b64 s[96:97], 0x2a818000
	s_mov_b32 m0, s81
	v_lshl_add_u64 v[240:241], v[240:241], 0, s[96:97]
	global_load_lds_dwordx4 v[240:241], off
	v_lshl_add_u64 v[240:241], v[94:95], 0, s[12:13]
	v_lshl_add_u64 v[240:241], v[240:241], 0, s[96:97]
	s_mov_b32 m0, s82
	s_mov_b64 s[96:97], 0x30e10000
	global_load_lds_dwordx4 v[240:241], off
	v_lshl_add_u64 v[240:241], v[90:91], 0, s[12:13]
	v_lshl_add_u64 v[240:241], v[240:241], 0, s[96:97]
	s_mov_b32 m0, s87
	s_nop 0
	global_load_lds_dwordx4 v[240:241], off
.Lmstag_2:
	v_exp_f32_e32 v43, v43
	v_exp_f32_e32 v44, v44
	v_exp_f32_e32 v45, v45
	v_exp_f32_e32 v46, v46
	v_exp_f32_e32 v47, v47
	v_exp_f32_e32 v48, v48
	v_exp_f32_e32 v49, v49
	v_mfma_f32_32x32x16_bf16 v[66:81], v[82:85], v[102:105], v[66:81]
	v_add_f32_e32 v0, 0, v184
	v_add_f32_e32 v0, v186, v0
	v_add_f32_e32 v0, v185, v0
	v_add_f32_e32 v0, v187, v0
	v_add_f32_e32 v0, v189, v0
	v_add_f32_e32 v0, v193, v0
	v_add_f32_e32 v0, v192, v0
	v_mfma_f32_32x32x16_bf16 v[50:65], v[86:89], v[102:105], v[50:65]
	ds_read_b128 v[82:85], v135
	ds_read_b128 v[86:89], v135 offset:8192
	v_add_f32_e32 v0, v194, v0
	v_add_f32_e32 v0, v188, v0
	v_add_f32_e32 v0, v191, v0
	v_add_f32_e32 v0, v190, v0
	v_add_f32_e32 v0, v196, v0
	v_add_f32_e32 v0, v195, v0
	s_waitcnt lgkmcnt(0)
	v_mfma_f32_32x32x16_bf16 v[66:81], v[82:85], v[106:109], v[66:81]
	v_add_f32_e32 v0, v198, v0
	v_add_f32_e32 v0, v197, v0
	v_add_f32_e32 v0, v199, v0
	v_add_f32_e32 v0, v34, v0
	v_add_f32_e32 v0, v35, v0
	v_add_f32_e32 v0, v36, v0
	v_add_f32_e32 v0, v37, v0
	v_mfma_f32_32x32x16_bf16 v[50:65], v[86:89], v[106:109], v[50:65]
	ds_read_b128 v[82:85], v136
	ds_read_b128 v[86:89], v136 offset:8192
	v_add_f32_e32 v0, v38, v0
	v_add_f32_e32 v0, v39, v0
	v_add_f32_e32 v0, v40, v0
	v_add_f32_e32 v0, v41, v0
	v_add_f32_e32 v0, v42, v0
	v_add_f32_e32 v0, v43, v0
	s_waitcnt lgkmcnt(0)
	v_mfma_f32_32x32x16_bf16 v[66:81], v[82:85], v[110:113], v[66:81]
	v_add_f32_e32 v0, v44, v0
	v_add_f32_e32 v0, v45, v0
	v_add_f32_e32 v0, v46, v0
	v_add_f32_e32 v0, v47, v0
	v_add_f32_e32 v0, v48, v0
	v_add_f32_e32 v0, v49, v0
	v_add_f32_e32 v145, v145, v0
	v_mfma_f32_32x32x16_bf16 v[50:65], v[86:89], v[110:113], v[50:65]
	ds_read_b128 v[82:85], v137
	ds_read_b128 v[86:89], v137 offset:8192
	s_waitcnt lgkmcnt(0)
	v_mfma_f32_32x32x16_bf16 v[66:81], v[82:85], v[114:117], v[66:81]
	v_mfma_f32_32x32x16_bf16 v[50:65], v[86:89], v[114:117], v[50:65]
	ds_read_b128 v[82:85], v138
	ds_read_b128 v[86:89], v138 offset:8192
	s_waitcnt lgkmcnt(0)
	v_mfma_f32_32x32x16_bf16 v[66:81], v[82:85], v[118:121], v[66:81]
	v_cvt_pk_bf16_f32 v82, v184, v186
	v_cvt_pk_bf16_f32 v83, v185, v187
	v_cvt_pk_bf16_f32 v84, v189, v193
	v_cvt_pk_bf16_f32 v85, v192, v194
	s_nop 0
	v_permlane32_swap_b32_e32 v82, v84
	v_mfma_f32_32x32x16_bf16 v[50:65], v[86:89], v[118:121], v[50:65]
	v_cvt_pk_bf16_f32 v86, v188, v191
	v_cvt_pk_bf16_f32 v87, v190, v196
	v_cvt_pk_bf16_f32 v88, v195, v198
	v_cvt_pk_bf16_f32 v89, v197, v199
	v_cvt_pk_bf16_f32 v122, v34, v35
	v_cvt_pk_bf16_f32 v123, v36, v37
	v_cvt_pk_bf16_f32 v124, v38, v39
	v_cvt_pk_bf16_f32 v125, v40, v41
	v_cvt_pk_bf16_f32 v150, v42, v43
	v_cvt_pk_bf16_f32 v151, v44, v45
	v_cvt_pk_bf16_f32 v152, v46, v47
	v_cvt_pk_bf16_f32 v153, v48, v49
	ds_read_b64_tr_b16 v[154:155], v139 offset:0
	ds_read_b64_tr_b16 v[156:157], v139 offset:0x400
	ds_read_b64_tr_b16 v[158:159], v139 offset:0x800
	ds_read_b64_tr_b16 v[160:161], v139 offset:0xc00
	ds_read_b64_tr_b16 v[162:163], v139 offset:0x1000
	ds_read_b64_tr_b16 v[164:165], v139 offset:0x1400
	ds_read_b64_tr_b16 v[166:167], v139 offset:0x1800
	ds_read_b64_tr_b16 v[168:169], v139 offset:0x1c00
	ds_read_b64_tr_b16 v[170:171], v139 offset:0x200
	ds_read_b64_tr_b16 v[172:173], v139 offset:0x600
	ds_read_b64_tr_b16 v[200:201], v139 offset:0xa00
	ds_read_b64_tr_b16 v[202:203], v139 offset:0xe00
	v_permlane32_swap_b32_e32 v83, v85
	ds_read_b64_tr_b16 v[204:205], v139 offset:0x1200
	ds_read_b64_tr_b16 v[206:207], v139 offset:0x1600
	ds_read_b64_tr_b16 v[208:209], v139 offset:0x1a00
	ds_read_b64_tr_b16 v[210:211], v139 offset:0x1e00
	s_waitcnt lgkmcnt(8)
	v_permlane32_swap_b32_e32 v86, v88
	s_nop 0
	v_mfma_f32_32x32x16_bf16 v[2:17], v[82:85], v[154:157], v[2:17]
	s_waitcnt lgkmcnt(0)
	v_permlane32_swap_b32_e32 v87, v89
	v_permlane32_swap_b32_e32 v122, v124
	v_permlane32_swap_b32_e32 v123, v125
	v_mfma_f32_32x32x16_bf16 v[18:33], v[82:85], v[170:173], v[18:33]
	v_permlane32_swap_b32_e32 v150, v152
	v_permlane32_swap_b32_e32 v151, v153
	v_exp_f32_e32 v170, v76
	v_exp_f32_e32 v171, v77
	v_exp_f32_e32 v172, v78
	v_mfma_f32_32x32x16_bf16 v[2:17], v[86:89], v[158:161], v[2:17]
	v_exp_f32_e32 v158, v66
	v_exp_f32_e32 v159, v67
	v_exp_f32_e32 v160, v68
	v_exp_f32_e32 v161, v69
	v_exp_f32_e32 v173, v79
	v_exp_f32_e32 v174, v80
	v_exp_f32_e32 v175, v81
	v_mfma_f32_32x32x16_bf16 v[18:33], v[86:89], v[200:203], v[18:33]
	v_mfma_f32_32x32x16_bf16 v[2:17], v[122:125], v[162:165], v[2:17]
	v_exp_f32_e32 v162, v70
	v_exp_f32_e32 v163, v71
	v_mfma_f32_32x32x16_bf16 v[18:33], v[122:125], v[204:207], v[18:33]
	v_mfma_f32_32x32x16_bf16 v[2:17], v[150:153], v[166:169], v[2:17]
	v_exp_f32_e32 v166, v72
	v_exp_f32_e32 v167, v73
	v_exp_f32_e32 v168, v74
	v_exp_f32_e32 v169, v75
	v_mfma_f32_32x32x16_bf16 v[18:33], v[150:153], v[208:211], v[18:33]
	s_andn2_b64 vcc, exec, s[0:1]
	s_cbranch_vccz .LBB0_1450

; __device__ __forceinline__ void finishSM(f32x16& p0, f32x16& p1, float& l_reg, bf16x8& pa0, bf16x8& pa1, bf16x8& pa2, bf16x8& pa3) {
; #pragma unroll
;   for (int r = 0; r < 16; ++r) p1[r] = __builtin_amdgcn_exp2f(p1[r]);
;   float ps = 0;
; #pragma unroll
;   for (int r = 0; r < 16; ++r) ps += p0[r];
; #pragma unroll
;   for (int r = 0; r < 16; ++r) ps += p1[r];
;   l_reg += ps;
;     ...
;   ATT_PK4(p0, 0, pa0); ATT_PK4(p0, 8, pa1); ATT_PK4(p1, 0, pa2); ATT_PK4(p1, 8, pa3);
;     ...
; }
; template <int DK>
; __device__ __forceinline__ void qkt(f32x16& p0, f32x16& p1, const char* Ks, const bf16x8* qr, int r32, int hi) {
;   p0 = f32x16{}; p1 = f32x16{};
; #pragma unroll
;   for (int d0 = 0; d0 < DK / 16; ++d0) { const int cb = (d0 * 16 + hi * 8) * 2;
;     const bf16x8 b0 = *reinterpret_cast<const bf16x8*>(Ks + ATT_KSWZ(r32, cb));
;     const bf16x8 b1 = *reinterpret_cast<const bf16x8*>(Ks + ATT_KSWZ(32 + r32, cb));
;     p0 = __builtin_amdgcn_mfma_f32_32x32x16_bf16(b0, qr[d0], p0, 0, 0, 0);
;     p1 = __builtin_amdgcn_mfma_f32_32x32x16_bf16(b1, qr[d0], p1, 0, 0, 0);
;   }
.LBB0_1456:
	ds_read_b128 v[34:37], v140
	ds_read_b128 v[38:41], v140 offset:8192
	ds_read_b128 v[82:85], v141
	ds_read_b128 v[86:89], v141 offset:8192
	v_exp_f32_e32 v50, v50
	v_exp_f32_e32 v51, v51
	s_waitcnt lgkmcnt(0)
	v_mfma_f32_32x32x16_bf16 v[66:81], v[34:37], v[98:101], 0
	v_exp_f32_e32 v52, v52
	v_exp_f32_e32 v53, v53
	v_exp_f32_e32 v54, v54
	v_exp_f32_e32 v55, v55
	v_exp_f32_e32 v56, v56
	v_exp_f32_e32 v57, v57
	v_exp_f32_e32 v58, v58
	v_mfma_f32_32x32x16_bf16 v[34:49], v[38:41], v[98:101], 0
	s_cmp_eq_u32 s93, 0
	s_cbranch_scc1 .Lmstag_3
	s_add_i32 s32, s92, 4
	s_cmp_ge_u32 s32, s89
	s_cbranch_scc1 .Lmstag_3
	v_lshl_add_u64 v[240:241], v[92:93], 0, s[12:13]
	s_mov_b64 s[96:97], 0x2a81b000
	s_mov_b32 m0, s83
	v_lshl_add_u64 v[240:241], v[240:241], 0, s[96:97]
	global_load_lds_dwordx4 v[240:241], off
	v_lshl_add_u64 v[240:241], v[94:95], 0, s[12:13]
	v_lshl_add_u64 v[240:241], v[240:241], 0, s[96:97]
	s_mov_b32 m0, s84
	s_mov_b64 s[96:97], 0x30e12000
	global_load_lds_dwordx4 v[240:241], off
	v_lshl_add_u64 v[240:241], v[90:91], 0, s[12:13]
	v_lshl_add_u64 v[240:241], v[240:241], 0, s[96:97]
	s_add_i32 m0, s87, 0x2000
	s_nop 0
	global_load_lds_dwordx4 v[240:241], off
.Lmstag_3:
	v_exp_f32_e32 v59, v59
	v_exp_f32_e32 v60, v60
	v_exp_f32_e32 v61, v61
	v_exp_f32_e32 v62, v62
	v_exp_f32_e32 v63, v63
	v_exp_f32_e32 v64, v64
	v_exp_f32_e32 v65, v65
	v_mfma_f32_32x32x16_bf16 v[66:81], v[82:85], v[102:105], v[66:81]
	v_add_f32_e32 v0, 0, v158
	v_add_f32_e32 v0, v159, v0
	v_add_f32_e32 v0, v160, v0
	v_add_f32_e32 v0, v161, v0
	v_add_f32_e32 v0, v162, v0
	v_add_f32_e32 v0, v163, v0
	v_add_f32_e32 v0, v166, v0
	v_mfma_f32_32x32x16_bf16 v[34:49], v[86:89], v[102:105], v[34:49]
	ds_read_b128 v[82:85], v142
	ds_read_b128 v[86:89], v142 offset:8192
	v_add_f32_e32 v0, v167, v0
	v_add_f32_e32 v0, v168, v0
	v_add_f32_e32 v0, v169, v0
	v_add_f32_e32 v0, v170, v0
	v_add_f32_e32 v0, v171, v0
	v_add_f32_e32 v0, v172, v0
	s_waitcnt lgkmcnt(0)
	v_mfma_f32_32x32x16_bf16 v[66:81], v[82:85], v[106:109], v[66:81]
	v_add_f32_e32 v0, v173, v0
	v_add_f32_e32 v0, v174, v0
	v_add_f32_e32 v0, v175, v0
	v_add_f32_e32 v0, v50, v0
	v_add_f32_e32 v0, v51, v0
	v_add_f32_e32 v0, v52, v0
	v_add_f32_e32 v0, v53, v0
	v_mfma_f32_32x32x16_bf16 v[34:49], v[86:89], v[106:109], v[34:49]
	ds_read_b128 v[82:85], v143
	ds_read_b128 v[86:89], v143 offset:8192
	v_add_f32_e32 v0, v54, v0
	v_add_f32_e32 v0, v55, v0
	v_add_f32_e32 v0, v56, v0
	v_add_f32_e32 v0, v57, v0
	v_add_f32_e32 v0, v58, v0
	v_add_f32_e32 v0, v59, v0
	s_waitcnt lgkmcnt(0)
	v_mfma_f32_32x32x16_bf16 v[66:81], v[82:85], v[110:113], v[66:81]
	v_add_f32_e32 v0, v60, v0
	v_add_f32_e32 v0, v61, v0
	v_add_f32_e32 v0, v62, v0
	v_add_f32_e32 v0, v63, v0
	v_add_f32_e32 v0, v64, v0
	v_add_f32_e32 v0, v65, v0
	v_add_f32_e32 v145, v145, v0
	v_mfma_f32_32x32x16_bf16 v[34:49], v[86:89], v[110:113], v[34:49]
	ds_read_b128 v[82:85], v144
	ds_read_b128 v[86:89], v144 offset:8192
	s_waitcnt lgkmcnt(0)
	v_mfma_f32_32x32x16_bf16 v[66:81], v[82:85], v[114:117], v[66:81]
	v_mfma_f32_32x32x16_bf16 v[34:49], v[86:89], v[114:117], v[34:49]
	ds_read_b128 v[82:85], v148
	ds_read_b128 v[86:89], v148 offset:8192
	s_waitcnt lgkmcnt(0)
	v_mfma_f32_32x32x16_bf16 v[66:81], v[82:85], v[118:121], v[66:81]
	v_cvt_pk_bf16_f32 v82, v158, v159
	v_cvt_pk_bf16_f32 v83, v160, v161
	v_cvt_pk_bf16_f32 v84, v162, v163
	v_cvt_pk_bf16_f32 v85, v166, v167
	s_nop 0
	v_permlane32_swap_b32_e32 v82, v84
	v_mfma_f32_32x32x16_bf16 v[34:49], v[86:89], v[118:121], v[34:49]
	v_cvt_pk_bf16_f32 v86, v168, v169
	v_cvt_pk_bf16_f32 v87, v170, v171
	v_cvt_pk_bf16_f32 v88, v172, v173
	v_cvt_pk_bf16_f32 v89, v174, v175
	v_cvt_pk_bf16_f32 v122, v50, v51
	v_cvt_pk_bf16_f32 v123, v52, v53
	v_cvt_pk_bf16_f32 v124, v54, v55
	v_cvt_pk_bf16_f32 v125, v56, v57
	v_cvt_pk_bf16_f32 v150, v58, v59
	v_cvt_pk_bf16_f32 v151, v60, v61
	v_cvt_pk_bf16_f32 v152, v62, v63
	v_cvt_pk_bf16_f32 v153, v64, v65
	ds_read_b64_tr_b16 v[154:155], v97 offset:0
	ds_read_b64_tr_b16 v[156:157], v97 offset:0x400
	ds_read_b64_tr_b16 v[184:185], v97 offset:0x800
	ds_read_b64_tr_b16 v[186:187], v97 offset:0xc00
	ds_read_b64_tr_b16 v[188:189], v97 offset:0x1000
	ds_read_b64_tr_b16 v[190:191], v97 offset:0x1400
	ds_read_b64_tr_b16 v[192:193], v97 offset:0x1800
	ds_read_b64_tr_b16 v[194:195], v97 offset:0x1c00
	ds_read_b64_tr_b16 v[196:197], v97 offset:0x200
	ds_read_b64_tr_b16 v[198:199], v97 offset:0x600
	ds_read_b64_tr_b16 v[200:201], v97 offset:0xa00
	ds_read_b64_tr_b16 v[202:203], v97 offset:0xe00
	v_permlane32_swap_b32_e32 v83, v85
	ds_read_b64_tr_b16 v[204:205], v97 offset:0x1200
	ds_read_b64_tr_b16 v[206:207], v97 offset:0x1600
	ds_read_b64_tr_b16 v[208:209], v97 offset:0x1a00
	ds_read_b64_tr_b16 v[210:211], v97 offset:0x1e00
	s_waitcnt lgkmcnt(8)
	v_permlane32_swap_b32_e32 v86, v88
	s_nop 0
	v_mfma_f32_32x32x16_bf16 v[2:17], v[82:85], v[154:157], v[2:17]
	s_waitcnt lgkmcnt(0)
	v_permlane32_swap_b32_e32 v87, v89
	v_permlane32_swap_b32_e32 v122, v124
	v_permlane32_swap_b32_e32 v123, v125
	v_mfma_f32_32x32x16_bf16 v[18:33], v[82:85], v[196:199], v[18:33]
	v_permlane32_swap_b32_e32 v150, v152
	v_permlane32_swap_b32_e32 v151, v153
	v_exp_f32_e32 v196, v77
	v_exp_f32_e32 v198, v79
	v_exp_f32_e32 v197, v80
	v_mfma_f32_32x32x16_bf16 v[2:17], v[86:89], v[184:187], v[2:17]
	v_exp_f32_e32 v184, v66
	v_exp_f32_e32 v186, v67
	v_exp_f32_e32 v185, v68
	v_exp_f32_e32 v187, v69
	v_exp_f32_e32 v199, v81
	v_mfma_f32_32x32x16_bf16 v[18:33], v[86:89], v[200:203], v[18:33]
	v_mfma_f32_32x32x16_bf16 v[2:17], v[122:125], v[188:191], v[2:17]
	v_exp_f32_e32 v189, v70
	v_exp_f32_e32 v188, v74
	v_exp_f32_e32 v191, v75
	v_exp_f32_e32 v190, v76
	v_mfma_f32_32x32x16_bf16 v[18:33], v[122:125], v[204:207], v[18:33]
	v_mfma_f32_32x32x16_bf16 v[2:17], v[150:153], v[192:195], v[2:17]
	v_exp_f32_e32 v193, v71
	v_exp_f32_e32 v192, v72
	v_exp_f32_e32 v194, v73
	v_exp_f32_e32 v195, v78
	v_mfma_f32_32x32x16_bf16 v[18:33], v[150:153], v[208:211], v[18:33]
	s_cmp_ge_u32 s92, s90
	s_cbranch_scc1 .LBB0_1433
